# plus non-temporal stores for the output-gate / memory-q tiles of the layer-0 in-projection (consumed three phases later)
# baseline (speedup 1.0000x reference)
.LBB0_380:
	s_waitcnt vmcnt(0)
	v_mul_f32_e32 v173, 0x3a800000, v138
	v_lshrrev_b32_e32 v138, 1, v152
	v_and_b32_e32 v152, 0x60, v138
	v_and_b32_e32 v174, 16, v138
	v_lshlrev_b32_e32 v138, 1, v152
	v_mul_f32_e32 v114, v114, v173
	v_lshl_add_u64 v[152:153], v[150:151], 0, v[138:139]
	v_mul_f32_e32 v150, 0xbfb8aa3b, v114
	v_exp_f32_e32 v175, v150
	v_lshlrev_b32_e32 v150, 1, v174
	v_mov_b32_e32 v151, v139
	v_mul_f32_e32 v115, v115, v173
	v_mul_f32_e32 v116, v116, v173
	v_lshl_add_u64 v[152:153], v[152:153], 0, v[150:151]
	v_add_f32_e32 v151, 1.0, v175
	v_mul_f32_e32 v174, 0xbfb8aa3b, v115
	v_mul_f32_e32 v175, 0xbfb8aa3b, v116
	v_exp_f32_e32 v174, v174
	v_exp_f32_e32 v175, v175
	v_mul_f32_e32 v117, v117, v173
	v_mul_f32_e32 v176, 0xbfb8aa3b, v117
	v_add_f32_e32 v174, 1.0, v174
	v_add_f32_e32 v175, 1.0, v175
	v_rcp_f32_e32 v151, v151
	v_rcp_f32_e32 v174, v174
	v_rcp_f32_e32 v175, v175
	v_exp_f32_e32 v176, v176
	v_mul_f32_e32 v118, v118, v173
	v_mul_f32_e32 v119, v119, v173
	v_cndmask_b32_e64 v114, v114, v151, s[6:7]
	v_cndmask_b32_e64 v115, v115, v174, s[6:7]
	v_cndmask_b32_e64 v116, v116, v175, s[6:7]
	v_add_f32_e32 v151, 1.0, v176
	v_mul_f32_e32 v174, 0xbfb8aa3b, v118
	v_mul_f32_e32 v175, 0xbfb8aa3b, v119
	v_rcp_f32_e32 v151, v151
	v_exp_f32_e32 v174, v174
	v_exp_f32_e32 v175, v175
	v_mul_f32_e32 v120, v120, v173
	v_mul_f32_e32 v121, v121, v173
	v_cndmask_b32_e64 v117, v117, v151, s[6:7]
	v_add_f32_e32 v151, 1.0, v174
	v_add_f32_e32 v174, 1.0, v175
	v_mul_f32_e32 v175, 0xbfb8aa3b, v120
	v_mul_f32_e32 v176, 0xbfb8aa3b, v121
	v_exp_f32_e32 v175, v175
	v_exp_f32_e32 v176, v176
	v_rcp_f32_e32 v151, v151
	v_rcp_f32_e32 v174, v174
	v_add_f32_e32 v175, 1.0, v175
	v_add_f32_e32 v176, 1.0, v176
	v_rcp_f32_e32 v175, v175
	v_rcp_f32_e32 v176, v176
	v_mul_f32_e32 v122, v122, v173
	v_cndmask_b32_e64 v118, v118, v151, s[6:7]
	v_cndmask_b32_e64 v119, v119, v174, s[6:7]
	v_cndmask_b32_e64 v120, v120, v175, s[6:7]
	v_cndmask_b32_e64 v121, v121, v176, s[6:7]
	v_cvt_pk_bf16_f32 v114, v114, v115
	v_cvt_pk_bf16_f32 v115, v116, v117
	v_mul_f32_e32 v116, 0xbfb8aa3b, v122
	v_exp_f32_e32 v151, v116
	v_cvt_pk_bf16_f32 v116, v118, v119
	v_cvt_pk_bf16_f32 v117, v120, v121
	global_store_dwordx4 v[152:153], v[114:117], off nt
	v_mul_f32_e32 v119, v125, v173
	v_mul_f32_e32 v120, 0xbfb8aa3b, v119
	v_mul_f32_e32 v115, v123, v173
	v_mul_f32_e32 v117, v124, v173
	v_mul_f32_e32 v116, 0xbfb8aa3b, v115
	v_mul_f32_e32 v118, 0xbfb8aa3b, v117
	v_exp_f32_e32 v116, v116
	v_exp_f32_e32 v118, v118
	v_add_f32_e32 v114, 1.0, v151
	v_rcp_f32_e32 v114, v114
	v_add_f32_e32 v116, 1.0, v116
	v_add_f32_e32 v118, 1.0, v118
	v_rcp_f32_e32 v116, v116
	v_rcp_f32_e32 v118, v118
	v_exp_f32_e32 v120, v120
	v_mul_f32_e32 v121, v127, v173
	v_cndmask_b32_e64 v115, v115, v116, s[6:7]
	v_cndmask_b32_e64 v116, v117, v118, s[6:7]
	v_mul_f32_e32 v118, v126, v173
	v_cndmask_b32_e64 v114, v122, v114, s[6:7]
	v_add_f32_e32 v117, 1.0, v120
	v_mul_f32_e32 v120, 0xbfb8aa3b, v118
	v_mul_f32_e32 v122, 0xbfb8aa3b, v121
	v_rcp_f32_e32 v117, v117
	v_exp_f32_e32 v120, v120
	v_exp_f32_e32 v122, v122
	v_mul_f32_e32 v124, v129, v173
	v_cndmask_b32_e64 v117, v119, v117, s[6:7]
	v_add_f32_e32 v119, 1.0, v120
	v_add_f32_e32 v120, 1.0, v122
	v_mul_f32_e32 v122, v128, v173
	v_mul_f32_e32 v123, 0xbfb8aa3b, v122
	v_mul_f32_e32 v125, 0xbfb8aa3b, v124
	v_exp_f32_e32 v123, v123
	v_exp_f32_e32 v125, v125
	v_rcp_f32_e32 v119, v119
	v_rcp_f32_e32 v120, v120
	v_add_f32_e32 v123, 1.0, v123
	v_add_f32_e32 v125, 1.0, v125
	v_rcp_f32_e32 v123, v123
	v_rcp_f32_e32 v125, v125
	v_mul_f32_e32 v98, v98, v173
	v_cndmask_b32_e64 v118, v118, v119, s[6:7]
	v_cndmask_b32_e64 v119, v121, v120, s[6:7]
	v_cndmask_b32_e64 v120, v122, v123, s[6:7]
	v_cndmask_b32_e64 v121, v124, v125, s[6:7]
	v_cvt_pk_bf16_f32 v114, v114, v115
	v_cvt_pk_bf16_f32 v115, v116, v117
	v_mul_f32_e32 v116, 0xbfb8aa3b, v98
	v_exp_f32_e32 v122, v116
	v_cvt_pk_bf16_f32 v116, v118, v119
	v_cvt_pk_bf16_f32 v117, v120, v121
	v_mul_f32_e32 v99, v99, v173
	v_mul_f32_e32 v100, v100, v173
	global_store_dwordx4 v[152:153], v[114:117], off offset:16 nt
	v_mul_f32_e32 v101, v101, v173
	v_mul_f32_e32 v102, v102, v173
	v_mul_f32_e32 v115, 0xbfb8aa3b, v99
	v_mul_f32_e32 v116, 0xbfb8aa3b, v100
	v_exp_f32_e32 v115, v115
	v_exp_f32_e32 v116, v116
	v_add_f32_e32 v114, 1.0, v122
	v_mul_f32_e32 v117, 0xbfb8aa3b, v101
	v_add_f32_e32 v115, 1.0, v115
	v_add_f32_e32 v116, 1.0, v116
	v_rcp_f32_e32 v114, v114
	v_rcp_f32_e32 v115, v115
	v_rcp_f32_e32 v116, v116
	v_exp_f32_e32 v117, v117
	v_mul_f32_e32 v103, v103, v173
	v_cndmask_b32_e64 v98, v98, v114, s[6:7]
	v_cndmask_b32_e64 v99, v99, v115, s[6:7]
	v_cndmask_b32_e64 v100, v100, v116, s[6:7]
	v_add_f32_e32 v114, 1.0, v117
	v_mul_f32_e32 v115, 0xbfb8aa3b, v102
	v_mul_f32_e32 v116, 0xbfb8aa3b, v103
	v_rcp_f32_e32 v114, v114
	v_exp_f32_e32 v115, v115
	v_exp_f32_e32 v116, v116
	v_mul_f32_e32 v104, v104, v173
	v_mul_f32_e32 v105, v105, v173
	v_cndmask_b32_e64 v101, v101, v114, s[6:7]
	v_add_f32_e32 v114, 1.0, v115
	v_add_f32_e32 v115, 1.0, v116
	v_mul_f32_e32 v116, 0xbfb8aa3b, v104
	v_mul_f32_e32 v117, 0xbfb8aa3b, v105
	v_exp_f32_e32 v116, v116
	v_exp_f32_e32 v117, v117
	v_rcp_f32_e32 v114, v114
	v_rcp_f32_e32 v115, v115
	v_add_f32_e32 v116, 1.0, v116
	v_add_f32_e32 v117, 1.0, v117
	v_rcp_f32_e32 v116, v116
	v_rcp_f32_e32 v117, v117
	v_mul_f32_e32 v106, v106, v173
	v_cndmask_b32_e64 v102, v102, v114, s[6:7]
	v_cndmask_b32_e64 v103, v103, v115, s[6:7]
	v_cndmask_b32_e64 v104, v104, v116, s[6:7]
	v_cndmask_b32_e64 v105, v105, v117, s[6:7]
	v_cvt_pk_bf16_f32 v98, v98, v99
	v_cvt_pk_bf16_f32 v99, v100, v101
	v_mul_f32_e32 v100, 0xbfb8aa3b, v106
	v_exp_f32_e32 v114, v100
	v_cvt_pk_bf16_f32 v100, v102, v103
	v_cvt_pk_bf16_f32 v101, v104, v105
	global_store_dwordx4 v[152:153], v[98:101], off offset:256 nt
	v_mul_f32_e32 v103, v109, v173
	v_mul_f32_e32 v104, 0xbfb8aa3b, v103
	v_mul_f32_e32 v99, v107, v173
	v_mul_f32_e32 v101, v108, v173
	v_mul_f32_e32 v100, 0xbfb8aa3b, v99
	v_mul_f32_e32 v102, 0xbfb8aa3b, v101
	v_exp_f32_e32 v100, v100
	v_exp_f32_e32 v102, v102
	v_add_f32_e32 v98, 1.0, v114
	v_rcp_f32_e32 v98, v98
	v_add_f32_e32 v100, 1.0, v100
	v_add_f32_e32 v102, 1.0, v102
	v_rcp_f32_e32 v100, v100
	v_rcp_f32_e32 v102, v102
	v_exp_f32_e32 v104, v104
	v_mul_f32_e32 v105, v111, v173
	v_cndmask_b32_e64 v99, v99, v100, s[6:7]
	v_cndmask_b32_e64 v100, v101, v102, s[6:7]
	v_mul_f32_e32 v102, v110, v173
	v_cndmask_b32_e64 v98, v106, v98, s[6:7]
	v_add_f32_e32 v101, 1.0, v104
	v_mul_f32_e32 v104, 0xbfb8aa3b, v102
	v_mul_f32_e32 v106, 0xbfb8aa3b, v105
	v_rcp_f32_e32 v101, v101
	v_exp_f32_e32 v104, v104
	v_exp_f32_e32 v106, v106
	v_mul_f32_e32 v108, v113, v173
	v_cndmask_b32_e64 v101, v103, v101, s[6:7]
	v_add_f32_e32 v103, 1.0, v104
	v_add_f32_e32 v104, 1.0, v106
	v_mul_f32_e32 v106, v112, v173
	v_mul_f32_e32 v107, 0xbfb8aa3b, v106
	v_mul_f32_e32 v109, 0xbfb8aa3b, v108
	v_exp_f32_e32 v107, v107
	v_exp_f32_e32 v109, v109
	v_rcp_f32_e32 v103, v103
	v_rcp_f32_e32 v104, v104
	v_add_f32_e32 v107, 1.0, v107
	v_add_f32_e32 v109, 1.0, v109
	v_rcp_f32_e32 v107, v107
	v_rcp_f32_e32 v109, v109
	v_cndmask_b32_e64 v102, v102, v103, s[6:7]
	v_cndmask_b32_e64 v103, v105, v104, s[6:7]
	v_cndmask_b32_e64 v104, v106, v107, s[6:7]
	v_cndmask_b32_e64 v105, v108, v109, s[6:7]
	v_cvt_pk_bf16_f32 v98, v98, v99
	v_cvt_pk_bf16_f32 v99, v100, v101
	v_cvt_pk_bf16_f32 v100, v102, v103
	v_cvt_pk_bf16_f32 v101, v104, v105
	global_store_dwordx4 v[152:153], v[98:101], off offset:272 nt
	s_andn2_b64 vcc, exec, s[38:39]
	s_nop 0
	v_cndmask_b32_e64 v100, 0, 1, s[38:39]
	v_or_b32_e32 v98, 32, v148
	v_mov_b32_e32 v99, v149
	v_cmp_ne_u32_e64 s[8:9], 1, v100
	s_mov_b64 s[38:39], -1
	s_cbranch_vccnz .LBB0_382
	v_lshlrev_b64 v[100:101], 10, v[98:99]
	v_lshl_add_u64 v[100:101], s[20:21], 0, v[100:101]
	v_lshl_add_u64 v[100:101], s[12:13], 1, v[100:101]
	s_mov_b64 s[38:39], 0

.LBB0_384:
	v_mul_f32_e32 v102, 0x3a800000, v172
	v_mul_f32_e32 v82, v82, v102
	v_mul_f32_e32 v98, 0xbfb8aa3b, v82
	v_exp_f32_e32 v103, v98
	v_mul_f32_e32 v83, v83, v102
	v_mul_f32_e32 v84, v84, v102
	v_lshl_add_u64 v[98:99], v[100:101], 0, v[138:139]
	v_add_f32_e32 v100, 1.0, v103
	v_mul_f32_e32 v101, 0xbfb8aa3b, v83
	v_mul_f32_e32 v103, 0xbfb8aa3b, v84
	v_exp_f32_e32 v101, v101
	v_exp_f32_e32 v103, v103
	v_mul_f32_e32 v85, v85, v102
	v_mul_f32_e32 v104, 0xbfb8aa3b, v85
	v_add_f32_e32 v101, 1.0, v101
	v_add_f32_e32 v103, 1.0, v103
	v_rcp_f32_e32 v100, v100
	v_rcp_f32_e32 v101, v101
	v_rcp_f32_e32 v103, v103
	v_exp_f32_e32 v104, v104
	v_mul_f32_e32 v86, v86, v102
	v_mul_f32_e32 v87, v87, v102
	v_cndmask_b32_e64 v82, v82, v100, s[6:7]
	v_cndmask_b32_e64 v83, v83, v101, s[6:7]
	v_cndmask_b32_e64 v84, v84, v103, s[6:7]
	v_add_f32_e32 v100, 1.0, v104
	v_mul_f32_e32 v101, 0xbfb8aa3b, v86
	v_mul_f32_e32 v103, 0xbfb8aa3b, v87
	v_rcp_f32_e32 v100, v100
	v_exp_f32_e32 v101, v101
	v_exp_f32_e32 v103, v103
	v_mul_f32_e32 v88, v88, v102
	v_mul_f32_e32 v89, v89, v102
	v_cndmask_b32_e64 v85, v85, v100, s[6:7]
	v_add_f32_e32 v100, 1.0, v101
	v_add_f32_e32 v101, 1.0, v103
	v_mul_f32_e32 v103, 0xbfb8aa3b, v88
	v_mul_f32_e32 v104, 0xbfb8aa3b, v89
	v_exp_f32_e32 v103, v103
	v_exp_f32_e32 v104, v104
	v_rcp_f32_e32 v100, v100
	v_rcp_f32_e32 v101, v101
	v_add_f32_e32 v103, 1.0, v103
	v_add_f32_e32 v104, 1.0, v104
	v_rcp_f32_e32 v103, v103
	v_rcp_f32_e32 v104, v104
	v_mul_f32_e32 v90, v90, v102
	v_mov_b32_e32 v151, v139
	v_cndmask_b32_e64 v86, v86, v100, s[6:7]
	v_cndmask_b32_e64 v87, v87, v101, s[6:7]
	v_cndmask_b32_e64 v88, v88, v103, s[6:7]
	v_cndmask_b32_e64 v89, v89, v104, s[6:7]
	v_cvt_pk_bf16_f32 v82, v82, v83
	v_cvt_pk_bf16_f32 v83, v84, v85
	v_mul_f32_e32 v84, 0xbfb8aa3b, v90
	v_lshl_add_u64 v[98:99], v[98:99], 0, v[150:151]
	v_exp_f32_e32 v100, v84
	v_cvt_pk_bf16_f32 v84, v86, v87
	v_cvt_pk_bf16_f32 v85, v88, v89
	global_store_dwordx4 v[98:99], v[82:85], off nt
	v_mul_f32_e32 v87, v93, v102
	v_mul_f32_e32 v88, 0xbfb8aa3b, v87
	v_mul_f32_e32 v83, v91, v102
	v_mul_f32_e32 v85, v92, v102
	v_mul_f32_e32 v84, 0xbfb8aa3b, v83
	v_mul_f32_e32 v86, 0xbfb8aa3b, v85
	v_exp_f32_e32 v84, v84
	v_exp_f32_e32 v86, v86
	v_add_f32_e32 v82, 1.0, v100
	v_rcp_f32_e32 v82, v82
	v_add_f32_e32 v84, 1.0, v84
	v_add_f32_e32 v86, 1.0, v86
	v_rcp_f32_e32 v84, v84
	v_rcp_f32_e32 v86, v86
	v_exp_f32_e32 v88, v88
	v_mul_f32_e32 v89, v95, v102
	v_cndmask_b32_e64 v83, v83, v84, s[6:7]
	v_cndmask_b32_e64 v84, v85, v86, s[6:7]
	v_mul_f32_e32 v86, v94, v102
	v_cndmask_b32_e64 v82, v90, v82, s[6:7]
	v_add_f32_e32 v85, 1.0, v88
	v_mul_f32_e32 v88, 0xbfb8aa3b, v86
	v_mul_f32_e32 v90, 0xbfb8aa3b, v89
	v_rcp_f32_e32 v85, v85
	v_exp_f32_e32 v88, v88
	v_exp_f32_e32 v90, v90
	v_mul_f32_e32 v92, v97, v102
	v_cndmask_b32_e64 v85, v87, v85, s[6:7]
	v_add_f32_e32 v87, 1.0, v88
	v_add_f32_e32 v88, 1.0, v90
	v_mul_f32_e32 v90, v96, v102
	v_mul_f32_e32 v91, 0xbfb8aa3b, v90
	v_mul_f32_e32 v93, 0xbfb8aa3b, v92
	v_exp_f32_e32 v91, v91
	v_exp_f32_e32 v93, v93
	v_rcp_f32_e32 v87, v87
	v_rcp_f32_e32 v88, v88
	v_add_f32_e32 v91, 1.0, v91
	v_add_f32_e32 v93, 1.0, v93
	v_rcp_f32_e32 v91, v91
	v_rcp_f32_e32 v93, v93
	v_mul_f32_e32 v66, v66, v102
	v_cndmask_b32_e64 v86, v86, v87, s[6:7]
	v_cndmask_b32_e64 v87, v89, v88, s[6:7]
	v_cndmask_b32_e64 v88, v90, v91, s[6:7]
	v_cndmask_b32_e64 v89, v92, v93, s[6:7]
	v_cvt_pk_bf16_f32 v82, v82, v83
	v_cvt_pk_bf16_f32 v83, v84, v85
	v_mul_f32_e32 v84, 0xbfb8aa3b, v66
	v_exp_f32_e32 v90, v84
	v_cvt_pk_bf16_f32 v84, v86, v87
	v_cvt_pk_bf16_f32 v85, v88, v89
	v_mul_f32_e32 v67, v67, v102
	v_mul_f32_e32 v68, v68, v102
	global_store_dwordx4 v[98:99], v[82:85], off offset:16 nt
	v_mul_f32_e32 v69, v69, v102
	v_mul_f32_e32 v70, v70, v102
	v_mul_f32_e32 v83, 0xbfb8aa3b, v67
	v_mul_f32_e32 v84, 0xbfb8aa3b, v68
	v_exp_f32_e32 v83, v83
	v_exp_f32_e32 v84, v84
	v_add_f32_e32 v82, 1.0, v90
	v_mul_f32_e32 v85, 0xbfb8aa3b, v69
	v_add_f32_e32 v83, 1.0, v83
	v_add_f32_e32 v84, 1.0, v84
	v_rcp_f32_e32 v82, v82
	v_rcp_f32_e32 v83, v83
	v_rcp_f32_e32 v84, v84
	v_exp_f32_e32 v85, v85
	v_mul_f32_e32 v71, v71, v102
	v_cndmask_b32_e64 v66, v66, v82, s[6:7]
	v_cndmask_b32_e64 v67, v67, v83, s[6:7]
	v_cndmask_b32_e64 v68, v68, v84, s[6:7]
	v_add_f32_e32 v82, 1.0, v85
	v_mul_f32_e32 v83, 0xbfb8aa3b, v70
	v_mul_f32_e32 v84, 0xbfb8aa3b, v71
	v_rcp_f32_e32 v82, v82
	v_exp_f32_e32 v83, v83
	v_exp_f32_e32 v84, v84
	v_mul_f32_e32 v72, v72, v102
	v_mul_f32_e32 v73, v73, v102
	v_cndmask_b32_e64 v69, v69, v82, s[6:7]
	v_add_f32_e32 v82, 1.0, v83
	v_add_f32_e32 v83, 1.0, v84
	v_mul_f32_e32 v84, 0xbfb8aa3b, v72
	v_mul_f32_e32 v85, 0xbfb8aa3b, v73
	v_exp_f32_e32 v84, v84
	v_exp_f32_e32 v85, v85
	v_rcp_f32_e32 v82, v82
	v_rcp_f32_e32 v83, v83
	v_add_f32_e32 v84, 1.0, v84
	v_add_f32_e32 v85, 1.0, v85
	v_rcp_f32_e32 v84, v84
	v_rcp_f32_e32 v85, v85
	v_mul_f32_e32 v74, v74, v102
	v_cndmask_b32_e64 v70, v70, v82, s[6:7]
	v_cndmask_b32_e64 v71, v71, v83, s[6:7]
	v_cndmask_b32_e64 v72, v72, v84, s[6:7]
	v_cndmask_b32_e64 v73, v73, v85, s[6:7]
	v_cvt_pk_bf16_f32 v66, v66, v67
	v_cvt_pk_bf16_f32 v67, v68, v69
	v_mul_f32_e32 v68, 0xbfb8aa3b, v74
	v_exp_f32_e32 v82, v68
	v_cvt_pk_bf16_f32 v68, v70, v71
	v_cvt_pk_bf16_f32 v69, v72, v73
	global_store_dwordx4 v[98:99], v[66:69], off offset:256 nt
	v_mul_f32_e32 v71, v77, v102
	v_mul_f32_e32 v72, 0xbfb8aa3b, v71
	v_mul_f32_e32 v67, v75, v102
	v_mul_f32_e32 v69, v76, v102
	v_mul_f32_e32 v68, 0xbfb8aa3b, v67
	v_mul_f32_e32 v70, 0xbfb8aa3b, v69
	v_exp_f32_e32 v68, v68
	v_exp_f32_e32 v70, v70
	v_add_f32_e32 v66, 1.0, v82
	v_rcp_f32_e32 v66, v66
	v_add_f32_e32 v68, 1.0, v68
	v_add_f32_e32 v70, 1.0, v70
	v_rcp_f32_e32 v68, v68
	v_rcp_f32_e32 v70, v70
	v_exp_f32_e32 v72, v72
	v_mul_f32_e32 v73, v79, v102
	v_cndmask_b32_e64 v67, v67, v68, s[6:7]
	v_cndmask_b32_e64 v68, v69, v70, s[6:7]
	v_mul_f32_e32 v70, v78, v102
	v_cndmask_b32_e64 v66, v74, v66, s[6:7]
	v_add_f32_e32 v69, 1.0, v72
	v_mul_f32_e32 v72, 0xbfb8aa3b, v70
	v_mul_f32_e32 v74, 0xbfb8aa3b, v73
	v_rcp_f32_e32 v69, v69
	v_exp_f32_e32 v72, v72
	v_exp_f32_e32 v74, v74
	v_mul_f32_e32 v76, v81, v102
	v_cndmask_b32_e64 v69, v71, v69, s[6:7]
	v_add_f32_e32 v71, 1.0, v72
	v_add_f32_e32 v72, 1.0, v74
	v_mul_f32_e32 v74, v80, v102
	v_mul_f32_e32 v75, 0xbfb8aa3b, v74
	v_mul_f32_e32 v77, 0xbfb8aa3b, v76
	v_exp_f32_e32 v75, v75
	v_exp_f32_e32 v77, v77
	v_rcp_f32_e32 v71, v71
	v_rcp_f32_e32 v72, v72
	v_add_f32_e32 v75, 1.0, v75
	v_add_f32_e32 v77, 1.0, v77
	v_rcp_f32_e32 v75, v75
	v_rcp_f32_e32 v77, v77
	v_cndmask_b32_e64 v70, v70, v71, s[6:7]
	v_cndmask_b32_e64 v71, v73, v72, s[6:7]
	v_cndmask_b32_e64 v72, v74, v75, s[6:7]
	v_cndmask_b32_e64 v73, v76, v77, s[6:7]
	v_cvt_pk_bf16_f32 v66, v66, v67
	v_cvt_pk_bf16_f32 v67, v68, v69
	v_cvt_pk_bf16_f32 v68, v70, v71
	v_cvt_pk_bf16_f32 v69, v72, v73
	global_store_dwordx4 v[98:99], v[66:69], off offset:272 nt
	s_and_b64 vcc, exec, s[8:9]
	s_mov_b64 s[38:39], -1
	v_lshl_add_u64 v[68:69], v[148:149], 0, s[16:17]
	s_cbranch_vccnz .LBB0_386
	v_lshlrev_b64 v[66:67], 10, v[68:69]
	v_lshl_add_u64 v[66:67], s[20:21], 0, v[66:67]
	v_lshl_add_u64 v[66:67], s[12:13], 1, v[66:67]
	s_mov_b64 s[38:39], 0

.LBB0_388:
	v_mul_f32_e32 v68, 0x3a800000, v171
	v_mul_f32_e32 v50, v50, v68
	v_mul_f32_e32 v51, v51, v68
	v_mul_f32_e32 v52, v52, v68
	v_mul_f32_e32 v69, 0xbfb8aa3b, v50
	v_mul_f32_e32 v70, 0xbfb8aa3b, v51
	v_mul_f32_e32 v71, 0xbfb8aa3b, v52
	v_exp_f32_e32 v69, v69
	v_exp_f32_e32 v70, v70
	v_exp_f32_e32 v71, v71
	v_mul_f32_e32 v53, v53, v68
	v_add_f32_e32 v69, 1.0, v69
	v_add_f32_e32 v70, 1.0, v70
	v_add_f32_e32 v71, 1.0, v71
	v_mul_f32_e32 v72, 0xbfb8aa3b, v53
	v_rcp_f32_e32 v69, v69
	v_rcp_f32_e32 v70, v70
	v_rcp_f32_e32 v71, v71
	v_exp_f32_e32 v72, v72
	v_mul_f32_e32 v54, v54, v68
	v_mul_f32_e32 v55, v55, v68
	v_cndmask_b32_e64 v50, v50, v69, s[6:7]
	v_cndmask_b32_e64 v51, v51, v70, s[6:7]
	v_cndmask_b32_e64 v52, v52, v71, s[6:7]
	v_add_f32_e32 v69, 1.0, v72
	v_mul_f32_e32 v70, 0xbfb8aa3b, v54
	v_mul_f32_e32 v71, 0xbfb8aa3b, v55
	v_rcp_f32_e32 v69, v69
	v_exp_f32_e32 v70, v70
	v_exp_f32_e32 v71, v71
	v_mul_f32_e32 v56, v56, v68
	v_mul_f32_e32 v57, v57, v68
	v_cndmask_b32_e64 v53, v53, v69, s[6:7]
	v_add_f32_e32 v69, 1.0, v70
	v_add_f32_e32 v70, 1.0, v71
	v_mul_f32_e32 v71, 0xbfb8aa3b, v56
	v_mul_f32_e32 v72, 0xbfb8aa3b, v57
	v_exp_f32_e32 v71, v71
	v_exp_f32_e32 v72, v72
	v_rcp_f32_e32 v69, v69
	v_rcp_f32_e32 v70, v70
	v_add_f32_e32 v71, 1.0, v71
	v_add_f32_e32 v72, 1.0, v72
	v_rcp_f32_e32 v71, v71
	v_rcp_f32_e32 v72, v72
	v_mul_f32_e32 v58, v58, v68
	v_lshl_add_u64 v[66:67], v[66:67], 0, v[138:139]
	v_mov_b32_e32 v151, v139
	v_cndmask_b32_e64 v54, v54, v69, s[6:7]
	v_cndmask_b32_e64 v55, v55, v70, s[6:7]
	v_cndmask_b32_e64 v56, v56, v71, s[6:7]
	v_cndmask_b32_e64 v57, v57, v72, s[6:7]
	v_cvt_pk_bf16_f32 v50, v50, v51
	v_cvt_pk_bf16_f32 v51, v52, v53
	v_mul_f32_e32 v52, 0xbfb8aa3b, v58
	v_lshl_add_u64 v[66:67], v[66:67], 0, v[150:151]
	v_exp_f32_e32 v69, v52
	v_cvt_pk_bf16_f32 v52, v54, v55
	v_cvt_pk_bf16_f32 v53, v56, v57
	global_store_dwordx4 v[66:67], v[50:53], off nt
	v_mul_f32_e32 v55, v61, v68
	v_mul_f32_e32 v56, 0xbfb8aa3b, v55
	v_mul_f32_e32 v51, v59, v68
	v_mul_f32_e32 v53, v60, v68
	v_mul_f32_e32 v52, 0xbfb8aa3b, v51
	v_mul_f32_e32 v54, 0xbfb8aa3b, v53
	v_exp_f32_e32 v52, v52
	v_exp_f32_e32 v54, v54
	v_add_f32_e32 v50, 1.0, v69
	v_rcp_f32_e32 v50, v50
	v_add_f32_e32 v52, 1.0, v52
	v_add_f32_e32 v54, 1.0, v54
	v_rcp_f32_e32 v52, v52
	v_rcp_f32_e32 v54, v54
	v_exp_f32_e32 v56, v56
	v_mul_f32_e32 v57, v63, v68
	v_cndmask_b32_e64 v51, v51, v52, s[6:7]
	v_cndmask_b32_e64 v52, v53, v54, s[6:7]
	v_mul_f32_e32 v54, v62, v68
	v_cndmask_b32_e64 v50, v58, v50, s[6:7]
	v_add_f32_e32 v53, 1.0, v56
	v_mul_f32_e32 v56, 0xbfb8aa3b, v54
	v_mul_f32_e32 v58, 0xbfb8aa3b, v57
	v_rcp_f32_e32 v53, v53
	v_exp_f32_e32 v56, v56
	v_exp_f32_e32 v58, v58
	v_mul_f32_e32 v60, v65, v68
	v_cndmask_b32_e64 v53, v55, v53, s[6:7]
	v_add_f32_e32 v55, 1.0, v56
	v_add_f32_e32 v56, 1.0, v58
	v_mul_f32_e32 v58, v64, v68
	v_mul_f32_e32 v59, 0xbfb8aa3b, v58
	v_mul_f32_e32 v61, 0xbfb8aa3b, v60
	v_exp_f32_e32 v59, v59
	v_exp_f32_e32 v61, v61
	v_rcp_f32_e32 v55, v55
	v_rcp_f32_e32 v56, v56
	v_add_f32_e32 v59, 1.0, v59
	v_add_f32_e32 v61, 1.0, v61
	v_rcp_f32_e32 v59, v59
	v_rcp_f32_e32 v61, v61
	v_mul_f32_e32 v34, v34, v68
	v_cndmask_b32_e64 v54, v54, v55, s[6:7]
	v_cndmask_b32_e64 v55, v57, v56, s[6:7]
	v_cndmask_b32_e64 v56, v58, v59, s[6:7]
	v_cndmask_b32_e64 v57, v60, v61, s[6:7]
	v_cvt_pk_bf16_f32 v50, v50, v51
	v_cvt_pk_bf16_f32 v51, v52, v53
	v_mul_f32_e32 v52, 0xbfb8aa3b, v34
	v_exp_f32_e32 v58, v52
	v_cvt_pk_bf16_f32 v52, v54, v55
	v_cvt_pk_bf16_f32 v53, v56, v57
	v_mul_f32_e32 v35, v35, v68
	v_mul_f32_e32 v36, v36, v68
	global_store_dwordx4 v[66:67], v[50:53], off offset:16 nt
	v_mul_f32_e32 v37, v37, v68
	v_mul_f32_e32 v38, v38, v68
	v_mul_f32_e32 v51, 0xbfb8aa3b, v35
	v_mul_f32_e32 v52, 0xbfb8aa3b, v36
	v_exp_f32_e32 v51, v51
	v_exp_f32_e32 v52, v52
	v_add_f32_e32 v50, 1.0, v58
	v_mul_f32_e32 v53, 0xbfb8aa3b, v37
	v_add_f32_e32 v51, 1.0, v51
	v_add_f32_e32 v52, 1.0, v52
	v_rcp_f32_e32 v50, v50
	v_rcp_f32_e32 v51, v51
	v_rcp_f32_e32 v52, v52
	v_exp_f32_e32 v53, v53
	v_mul_f32_e32 v39, v39, v68
	v_cndmask_b32_e64 v34, v34, v50, s[6:7]
	v_cndmask_b32_e64 v35, v35, v51, s[6:7]
	v_cndmask_b32_e64 v36, v36, v52, s[6:7]
	v_add_f32_e32 v50, 1.0, v53
	v_mul_f32_e32 v51, 0xbfb8aa3b, v38
	v_mul_f32_e32 v52, 0xbfb8aa3b, v39
	v_rcp_f32_e32 v50, v50
	v_exp_f32_e32 v51, v51
	v_exp_f32_e32 v52, v52
	v_mul_f32_e32 v40, v40, v68
	v_mul_f32_e32 v41, v41, v68
	v_cndmask_b32_e64 v37, v37, v50, s[6:7]
	v_add_f32_e32 v50, 1.0, v51
	v_add_f32_e32 v51, 1.0, v52
	v_mul_f32_e32 v52, 0xbfb8aa3b, v40
	v_mul_f32_e32 v53, 0xbfb8aa3b, v41
	v_exp_f32_e32 v52, v52
	v_exp_f32_e32 v53, v53
	v_rcp_f32_e32 v50, v50
	v_rcp_f32_e32 v51, v51
	v_add_f32_e32 v52, 1.0, v52
	v_add_f32_e32 v53, 1.0, v53
	v_rcp_f32_e32 v52, v52
	v_rcp_f32_e32 v53, v53
	v_mul_f32_e32 v42, v42, v68
	v_cndmask_b32_e64 v38, v38, v50, s[6:7]
	v_cndmask_b32_e64 v39, v39, v51, s[6:7]
	v_cndmask_b32_e64 v40, v40, v52, s[6:7]
	v_cndmask_b32_e64 v41, v41, v53, s[6:7]
	v_cvt_pk_bf16_f32 v34, v34, v35
	v_cvt_pk_bf16_f32 v35, v36, v37
	v_mul_f32_e32 v36, 0xbfb8aa3b, v42
	v_exp_f32_e32 v50, v36
	v_cvt_pk_bf16_f32 v36, v38, v39
	v_cvt_pk_bf16_f32 v37, v40, v41
	global_store_dwordx4 v[66:67], v[34:37], off offset:256 nt
	v_mul_f32_e32 v39, v45, v68
	v_mul_f32_e32 v40, 0xbfb8aa3b, v39
	v_mul_f32_e32 v35, v43, v68
	v_mul_f32_e32 v37, v44, v68
	v_mul_f32_e32 v36, 0xbfb8aa3b, v35
	v_mul_f32_e32 v38, 0xbfb8aa3b, v37
	v_exp_f32_e32 v36, v36
	v_exp_f32_e32 v38, v38
	v_add_f32_e32 v34, 1.0, v50
	v_rcp_f32_e32 v34, v34
	v_add_f32_e32 v36, 1.0, v36
	v_add_f32_e32 v38, 1.0, v38
	v_rcp_f32_e32 v36, v36
	v_rcp_f32_e32 v38, v38
	v_exp_f32_e32 v40, v40
	v_mul_f32_e32 v41, v47, v68
	v_cndmask_b32_e64 v35, v35, v36, s[6:7]
	v_cndmask_b32_e64 v36, v37, v38, s[6:7]
	v_mul_f32_e32 v38, v46, v68
	v_cndmask_b32_e64 v34, v42, v34, s[6:7]
	v_add_f32_e32 v37, 1.0, v40
	v_mul_f32_e32 v40, 0xbfb8aa3b, v38
	v_mul_f32_e32 v42, 0xbfb8aa3b, v41
	v_rcp_f32_e32 v37, v37
	v_exp_f32_e32 v40, v40
	v_exp_f32_e32 v42, v42
	v_mul_f32_e32 v44, v49, v68
	v_cndmask_b32_e64 v37, v39, v37, s[6:7]
	v_add_f32_e32 v39, 1.0, v40
	v_add_f32_e32 v40, 1.0, v42
	v_mul_f32_e32 v42, v48, v68
	v_mul_f32_e32 v43, 0xbfb8aa3b, v42
	v_mul_f32_e32 v45, 0xbfb8aa3b, v44
	v_exp_f32_e32 v43, v43
	v_exp_f32_e32 v45, v45
	v_rcp_f32_e32 v39, v39
	v_rcp_f32_e32 v40, v40
	v_add_f32_e32 v43, 1.0, v43
	v_add_f32_e32 v45, 1.0, v45
	v_rcp_f32_e32 v43, v43
	v_rcp_f32_e32 v45, v45
	v_cndmask_b32_e64 v38, v38, v39, s[6:7]
	v_cndmask_b32_e64 v39, v41, v40, s[6:7]
	v_cndmask_b32_e64 v40, v42, v43, s[6:7]
	v_cndmask_b32_e64 v41, v44, v45, s[6:7]
	v_cvt_pk_bf16_f32 v34, v34, v35
	v_cvt_pk_bf16_f32 v35, v36, v37
	v_cvt_pk_bf16_f32 v36, v38, v39
	v_cvt_pk_bf16_f32 v37, v40, v41
	global_store_dwordx4 v[66:67], v[34:37], off offset:272 nt
	s_and_b64 vcc, exec, s[8:9]
	s_mov_b64 s[8:9], -1
	v_lshl_add_u64 v[36:37], v[148:149], 0, s[24:25]
	s_cbranch_vccnz .LBB0_390
	v_lshlrev_b64 v[34:35], 10, v[36:37]
	v_lshl_add_u64 v[34:35], s[20:21], 0, v[34:35]
	v_lshl_add_u64 v[34:35], s[12:13], 1, v[34:35]
	s_mov_b64 s[8:9], 0

.LBB0_392:
	v_mul_f32_e32 v36, 0x3a800000, v170
	v_mul_f32_e32 v18, v18, v36
	v_mul_f32_e32 v19, v19, v36
	v_mul_f32_e32 v20, v20, v36
	v_mul_f32_e32 v37, 0xbfb8aa3b, v18
	v_mul_f32_e32 v38, 0xbfb8aa3b, v19
	v_mul_f32_e32 v39, 0xbfb8aa3b, v20
	v_exp_f32_e32 v37, v37
	v_exp_f32_e32 v38, v38
	v_exp_f32_e32 v39, v39
	v_mul_f32_e32 v21, v21, v36
	v_add_f32_e32 v37, 1.0, v37
	v_add_f32_e32 v38, 1.0, v38
	v_add_f32_e32 v39, 1.0, v39
	v_mul_f32_e32 v40, 0xbfb8aa3b, v21
	v_rcp_f32_e32 v37, v37
	v_rcp_f32_e32 v38, v38
	v_rcp_f32_e32 v39, v39
	v_exp_f32_e32 v40, v40
	v_mul_f32_e32 v22, v22, v36
	v_mul_f32_e32 v23, v23, v36
	v_cndmask_b32_e64 v18, v18, v37, s[6:7]
	v_cndmask_b32_e64 v19, v19, v38, s[6:7]
	v_cndmask_b32_e64 v20, v20, v39, s[6:7]
	v_add_f32_e32 v37, 1.0, v40
	v_mul_f32_e32 v38, 0xbfb8aa3b, v22
	v_mul_f32_e32 v39, 0xbfb8aa3b, v23
	v_rcp_f32_e32 v37, v37
	v_exp_f32_e32 v38, v38
	v_exp_f32_e32 v39, v39
	v_mul_f32_e32 v24, v24, v36
	v_mul_f32_e32 v25, v25, v36
	v_cndmask_b32_e64 v21, v21, v37, s[6:7]
	v_add_f32_e32 v37, 1.0, v38
	v_add_f32_e32 v38, 1.0, v39
	v_mul_f32_e32 v39, 0xbfb8aa3b, v24
	v_mul_f32_e32 v40, 0xbfb8aa3b, v25
	v_exp_f32_e32 v39, v39
	v_exp_f32_e32 v40, v40
	v_rcp_f32_e32 v37, v37
	v_rcp_f32_e32 v38, v38
	v_add_f32_e32 v39, 1.0, v39
	v_add_f32_e32 v40, 1.0, v40
	v_rcp_f32_e32 v39, v39
	v_rcp_f32_e32 v40, v40
	v_mul_f32_e32 v26, v26, v36
	v_lshl_add_u64 v[34:35], v[34:35], 0, v[138:139]
	v_mov_b32_e32 v151, v139
	v_cndmask_b32_e64 v22, v22, v37, s[6:7]
	v_cndmask_b32_e64 v23, v23, v38, s[6:7]
	v_cndmask_b32_e64 v24, v24, v39, s[6:7]
	v_cndmask_b32_e64 v25, v25, v40, s[6:7]
	v_cvt_pk_bf16_f32 v18, v18, v19
	v_cvt_pk_bf16_f32 v19, v20, v21
	v_mul_f32_e32 v20, 0xbfb8aa3b, v26
	v_lshl_add_u64 v[34:35], v[34:35], 0, v[150:151]
	v_exp_f32_e32 v37, v20
	v_cvt_pk_bf16_f32 v20, v22, v23
	v_cvt_pk_bf16_f32 v21, v24, v25
	global_store_dwordx4 v[34:35], v[18:21], off nt
	v_mul_f32_e32 v23, v29, v36
	v_mul_f32_e32 v24, 0xbfb8aa3b, v23
	v_mul_f32_e32 v19, v27, v36
	v_mul_f32_e32 v21, v28, v36
	v_mul_f32_e32 v20, 0xbfb8aa3b, v19
	v_mul_f32_e32 v22, 0xbfb8aa3b, v21
	v_exp_f32_e32 v20, v20
	v_exp_f32_e32 v22, v22
	v_add_f32_e32 v18, 1.0, v37
	v_rcp_f32_e32 v18, v18
	v_add_f32_e32 v20, 1.0, v20
	v_add_f32_e32 v22, 1.0, v22
	v_rcp_f32_e32 v20, v20
	v_rcp_f32_e32 v22, v22
	v_exp_f32_e32 v24, v24
	v_mul_f32_e32 v25, v31, v36
	v_cndmask_b32_e64 v19, v19, v20, s[6:7]
	v_cndmask_b32_e64 v20, v21, v22, s[6:7]
	v_mul_f32_e32 v22, v30, v36
	v_cndmask_b32_e64 v18, v26, v18, s[6:7]
	v_add_f32_e32 v21, 1.0, v24
	v_mul_f32_e32 v24, 0xbfb8aa3b, v22
	v_mul_f32_e32 v26, 0xbfb8aa3b, v25
	v_rcp_f32_e32 v21, v21
	v_exp_f32_e32 v24, v24
	v_exp_f32_e32 v26, v26
	v_mul_f32_e32 v28, v33, v36
	v_cndmask_b32_e64 v21, v23, v21, s[6:7]
	v_add_f32_e32 v23, 1.0, v24
	v_add_f32_e32 v24, 1.0, v26
	v_mul_f32_e32 v26, v32, v36
	v_mul_f32_e32 v27, 0xbfb8aa3b, v26
	v_mul_f32_e32 v29, 0xbfb8aa3b, v28
	v_exp_f32_e32 v27, v27
	v_exp_f32_e32 v29, v29
	v_rcp_f32_e32 v23, v23
	v_rcp_f32_e32 v24, v24
	v_add_f32_e32 v27, 1.0, v27
	v_add_f32_e32 v29, 1.0, v29
	v_rcp_f32_e32 v27, v27
	v_rcp_f32_e32 v29, v29
	v_mul_f32_e32 v2, v2, v36
	v_cndmask_b32_e64 v22, v22, v23, s[6:7]
	v_cndmask_b32_e64 v23, v25, v24, s[6:7]
	v_cndmask_b32_e64 v24, v26, v27, s[6:7]
	v_cndmask_b32_e64 v25, v28, v29, s[6:7]
	v_cvt_pk_bf16_f32 v18, v18, v19
	v_cvt_pk_bf16_f32 v19, v20, v21
	v_mul_f32_e32 v20, 0xbfb8aa3b, v2
	v_exp_f32_e32 v26, v20
	v_cvt_pk_bf16_f32 v20, v22, v23
	v_cvt_pk_bf16_f32 v21, v24, v25
	v_mul_f32_e32 v3, v3, v36
	v_mul_f32_e32 v4, v4, v36
	global_store_dwordx4 v[34:35], v[18:21], off offset:16 nt
	v_mul_f32_e32 v5, v5, v36
	v_mul_f32_e32 v6, v6, v36
	v_mul_f32_e32 v19, 0xbfb8aa3b, v3
	v_mul_f32_e32 v20, 0xbfb8aa3b, v4
	v_exp_f32_e32 v19, v19
	v_exp_f32_e32 v20, v20
	v_add_f32_e32 v18, 1.0, v26
	v_mul_f32_e32 v21, 0xbfb8aa3b, v5
	v_add_f32_e32 v19, 1.0, v19
	v_add_f32_e32 v20, 1.0, v20
	v_rcp_f32_e32 v18, v18
	v_rcp_f32_e32 v19, v19
	v_rcp_f32_e32 v20, v20
	v_exp_f32_e32 v21, v21
	v_mul_f32_e32 v7, v7, v36
	v_cndmask_b32_e64 v2, v2, v18, s[6:7]
	v_cndmask_b32_e64 v3, v3, v19, s[6:7]
	v_cndmask_b32_e64 v4, v4, v20, s[6:7]
	v_add_f32_e32 v18, 1.0, v21
	v_mul_f32_e32 v19, 0xbfb8aa3b, v6
	v_mul_f32_e32 v20, 0xbfb8aa3b, v7
	v_rcp_f32_e32 v18, v18
	v_exp_f32_e32 v19, v19
	v_exp_f32_e32 v20, v20
	v_mul_f32_e32 v8, v8, v36
	v_mul_f32_e32 v9, v9, v36
	v_cndmask_b32_e64 v5, v5, v18, s[6:7]
	v_add_f32_e32 v18, 1.0, v19
	v_add_f32_e32 v19, 1.0, v20
	v_mul_f32_e32 v20, 0xbfb8aa3b, v8
	v_mul_f32_e32 v21, 0xbfb8aa3b, v9
	v_exp_f32_e32 v20, v20
	v_exp_f32_e32 v21, v21
	v_rcp_f32_e32 v18, v18
	v_rcp_f32_e32 v19, v19
	v_add_f32_e32 v20, 1.0, v20
	v_add_f32_e32 v21, 1.0, v21
	v_rcp_f32_e32 v20, v20
	v_rcp_f32_e32 v21, v21
	v_mul_f32_e32 v10, v10, v36
	v_cndmask_b32_e64 v6, v6, v18, s[6:7]
	v_cndmask_b32_e64 v7, v7, v19, s[6:7]
	v_cndmask_b32_e64 v8, v8, v20, s[6:7]
	v_cndmask_b32_e64 v9, v9, v21, s[6:7]
	v_cvt_pk_bf16_f32 v2, v2, v3
	v_cvt_pk_bf16_f32 v3, v4, v5
	v_mul_f32_e32 v4, 0xbfb8aa3b, v10
	v_exp_f32_e32 v18, v4
	v_cvt_pk_bf16_f32 v4, v6, v7
	v_cvt_pk_bf16_f32 v5, v8, v9
	global_store_dwordx4 v[34:35], v[2:5], off offset:256 nt
	v_mul_f32_e32 v7, v13, v36
	v_mul_f32_e32 v8, 0xbfb8aa3b, v7
	v_mul_f32_e32 v3, v11, v36
	v_mul_f32_e32 v5, v12, v36
	v_mul_f32_e32 v4, 0xbfb8aa3b, v3
	v_mul_f32_e32 v6, 0xbfb8aa3b, v5
	v_exp_f32_e32 v4, v4
	v_exp_f32_e32 v6, v6
	v_add_f32_e32 v2, 1.0, v18
	v_rcp_f32_e32 v2, v2
	v_add_f32_e32 v4, 1.0, v4
	v_add_f32_e32 v6, 1.0, v6
	v_rcp_f32_e32 v4, v4
	v_rcp_f32_e32 v6, v6
	v_exp_f32_e32 v8, v8
	v_mul_f32_e32 v9, v15, v36
	v_cndmask_b32_e64 v3, v3, v4, s[6:7]
	v_cndmask_b32_e64 v4, v5, v6, s[6:7]
	v_mul_f32_e32 v6, v14, v36
	v_cndmask_b32_e64 v2, v10, v2, s[6:7]
	v_add_f32_e32 v5, 1.0, v8
	v_mul_f32_e32 v8, 0xbfb8aa3b, v6
	v_mul_f32_e32 v10, 0xbfb8aa3b, v9
	v_rcp_f32_e32 v5, v5
	v_exp_f32_e32 v8, v8
	v_exp_f32_e32 v10, v10
	v_mul_f32_e32 v12, v17, v36
	v_cndmask_b32_e64 v5, v7, v5, s[6:7]
	v_add_f32_e32 v7, 1.0, v8
	v_add_f32_e32 v8, 1.0, v10
	v_mul_f32_e32 v10, v16, v36
	v_mul_f32_e32 v11, 0xbfb8aa3b, v10
	v_mul_f32_e32 v13, 0xbfb8aa3b, v12
	v_exp_f32_e32 v11, v11
	v_exp_f32_e32 v13, v13
	v_rcp_f32_e32 v7, v7
	v_rcp_f32_e32 v8, v8
	v_add_f32_e32 v11, 1.0, v11
	v_add_f32_e32 v13, 1.0, v13
	v_rcp_f32_e32 v11, v11
	v_rcp_f32_e32 v13, v13
	v_cndmask_b32_e64 v6, v6, v7, s[6:7]
	v_cndmask_b32_e64 v7, v9, v8, s[6:7]
	v_cndmask_b32_e64 v8, v10, v11, s[6:7]
	v_cndmask_b32_e64 v9, v12, v13, s[6:7]
	v_cvt_pk_bf16_f32 v2, v2, v3
	v_cvt_pk_bf16_f32 v3, v4, v5
	v_cvt_pk_bf16_f32 v4, v6, v7
	v_cvt_pk_bf16_f32 v5, v8, v9
	global_store_dwordx4 v[34:35], v[2:5], off offset:272 nt
	s_andn2_b64 vcc, exec, s[4:5]
	s_mov_b64 s[4:5], -1
	s_cbranch_vccnz .LBB0_365
	s_andn2_b64 vcc, exec, s[14:15]
	s_cbranch_vccnz .LBB0_364
	s_barrier
	s_branch .LBB0_364
